# vt8fuse + ropededup: the bj=1 rope blocks of the layer-1 QKV epilogue reuse the cos/sin values their bj=0 block loaded (same addresses) instead of reloading behind a full wait
# baseline (speedup 1.0000x reference)
.LBB0_973:
	s_and_b32 s98, s46, 3
	s_lshl_b32 s98, s98, 1
	s_mov_b32 s99, s47
	v_and_b32_e32 v250, 63, v0
	v_and_b32_e32 v251, 15, v250
	v_lshrrev_b32_e32 v249, 4, v250
	v_readfirstlane_b32 s100, v0
	s_lshr_b32 s100, s100, 6
	s_lshl_b32 s101, s100, 11
	s_add_i32 s101, s101, 0xc000
	v_lshl_add_u32 v245, v250, 4, s101
	v_lshrrev_b32_e32 v248, 2, v251
	v_xor_b32_e32 v248, v248, v249
	v_and_b32_e32 v248, 1, v248
	v_lshlrev_b32_e32 v248, 5, v248
	v_lshl_add_u32 v248, v249, 9, v248
	v_and_b32_e32 v247, 3, v251
	v_add_u32_e32 v248, v248, v247
	v_lshrrev_b32_e32 v247, 3, v251
	v_lshl_add_u32 v248, v247, 2, v248
	v_add_u32_e32 v244, s101, v248
	s_and_b32 s101, s100, 3
	s_lshl_b32 s101, s101, 11
	v_lshl_add_u32 v252, v250, 4, s101
	s_ashr_i32 s6, s46, 2
	s_cmp_gt_i32 s6, 1
	s_cselect_b64 s[42:43], -1, 0
	s_cmp_lt_i32 s6, 2
	v_lshl_add_u32 v6, s47, 8, v200
	s_cselect_b64 s[4:5], -1, 0
	s_cmpk_lt_i32 s47, 0x80
	v_lshrrev_b32_e32 v2, 1, v201
	s_cselect_b64 s[44:45], -1, 0
	v_and_b32_e32 v30, 28, v2
	v_lshlrev_b32_e32 v2, 5, v6
	v_and_or_b32 v2, v2, s64, v30
	s_and_b64 s[44:45], s[4:5], s[44:45]
	v_lshlrev_b32_e32 v194, 3, v2
	v_cndmask_b32_e64 v2, 0, 1, s[44:45]
	v_pk_mul_f32 v[24:25], v[192:193], s[28:29] op_sel_hi:[1,0]
	v_pk_mul_f32 v[18:19], v[190:191], s[28:29] op_sel_hi:[1,0]
	v_pk_mul_f32 v[22:23], v[188:189], s[28:29] op_sel_hi:[1,0]
	v_pk_mul_f32 v[20:21], v[186:187], s[28:29] op_sel_hi:[1,0]
	v_cmp_ne_u32_e64 s[4:5], 1, v2
	s_andn2_b64 vcc, exec, s[44:45]
	v_lshl_add_u64 v[14:15], s[18:19], 0, v[194:195]
	s_cbranch_vccnz .LBB0_975
	global_load_dwordx4 v[2:5], v[14:15], off
	global_load_dwordx4 v[8:11], v[14:15], off offset:16
	s_waitcnt vmcnt(1)
	v_mov_b32_e32 v224, v2
	v_mov_b32_e32 v225, v3
	v_mov_b32_e32 v226, v4
	v_mov_b32_e32 v227, v5
	v_pk_mul_f32 v[16:17], v[18:19], v[2:3] op_sel:[1,1] op_sel_hi:[1,0]
	v_mul_f32_e32 v32, v25, v5
	v_mul_f32_e32 v34, v25, v4
	s_waitcnt vmcnt(0)
	v_mov_b32_e32 v228, v8
	v_mov_b32_e32 v229, v9
	v_mov_b32_e32 v230, v10
	v_mov_b32_e32 v231, v11
	v_pk_mul_f32 v[38:39], v[20:21], v[8:9] op_sel:[1,1] op_sel_hi:[1,0]
	v_mul_f32_e32 v40, v23, v11
	v_mul_f32_e32 v42, v23, v10
	v_pk_mul_f32 v[12:13], v[18:19], v[2:3]
	v_pk_mul_f32 v[36:37], v[20:21], v[8:9]
	v_pk_fma_f32 v[18:19], v[18:19], v[2:3], v[16:17] op_sel_hi:[0,1,1]
	v_pk_fma_f32 v[2:3], v[24:25], v[4:5], v[32:33] op_sel_hi:[1,1,0] neg_lo:[0,0,1] neg_hi:[0,0,1]
	v_pk_fma_f32 v[4:5], v[24:25], v[4:5], v[34:35] op_sel:[0,1,0] op_sel_hi:[1,0,0]
	v_pk_fma_f32 v[20:21], v[20:21], v[8:9], v[38:39] op_sel_hi:[0,1,1]
	v_pk_fma_f32 v[8:9], v[22:23], v[10:11], v[40:41] op_sel_hi:[1,1,0] neg_lo:[0,0,1] neg_hi:[0,0,1]
	v_pk_fma_f32 v[10:11], v[22:23], v[10:11], v[42:43] op_sel:[0,1,0] op_sel_hi:[1,0,0]
	v_sub_f32_e32 v20, v36, v38
	v_sub_f32_e32 v18, v12, v16
	v_mov_b32_e32 v22, v8
	v_mov_b32_e32 v23, v10
	v_mov_b32_e32 v24, v2
	v_mov_b32_e32 v25, v4

.LBB0_979:
	v_pk_mul_f32 v[22:23], v[184:185], s[28:29] op_sel_hi:[1,0]
	v_pk_mul_f32 v[18:19], v[182:183], s[28:29] op_sel_hi:[1,0]
	v_pk_mul_f32 v[20:21], v[180:181], s[28:29] op_sel_hi:[1,0]
	s_and_b64 vcc, exec, s[4:5]
	v_pk_mul_f32 v[24:25], v[178:179], s[28:29] op_sel_hi:[1,0]
	s_cbranch_vccnz .LBB0_981
	v_mov_b32_e32 v32, v224
	v_mov_b32_e32 v33, v225
	v_mov_b32_e32 v34, v226
	v_mov_b32_e32 v35, v227
	v_mov_b32_e32 v36, v228
	v_mov_b32_e32 v37, v229
	v_mov_b32_e32 v38, v230
	v_mov_b32_e32 v39, v231
	v_pk_mul_f32 v[40:41], v[18:19], v[32:33] op_sel:[1,1] op_sel_hi:[1,0]
	v_mul_f32_e32 v42, v23, v35
	v_mul_f32_e32 v44, v23, v34
	v_pk_mul_f32 v[48:49], v[24:25], v[36:37] op_sel:[1,1] op_sel_hi:[1,0]
	v_mul_f32_e32 v50, v21, v39
	v_mul_f32_e32 v52, v21, v38
	v_pk_mul_f32 v[14:15], v[18:19], v[32:33]
	v_pk_mul_f32 v[46:47], v[24:25], v[36:37]
	v_pk_fma_f32 v[18:19], v[18:19], v[32:33], v[40:41] op_sel_hi:[0,1,1]
	v_pk_fma_f32 v[32:33], v[22:23], v[34:35], v[42:43] op_sel_hi:[1,1,0] neg_lo:[0,0,1] neg_hi:[0,0,1]
	v_pk_fma_f32 v[34:35], v[22:23], v[34:35], v[44:45] op_sel:[0,1,0] op_sel_hi:[1,0,0]
	v_pk_fma_f32 v[24:25], v[24:25], v[36:37], v[48:49] op_sel_hi:[0,1,1]
	v_pk_fma_f32 v[22:23], v[20:21], v[38:39], v[50:51] op_sel_hi:[1,1,0] neg_lo:[0,0,1] neg_hi:[0,0,1]
	v_pk_fma_f32 v[36:37], v[20:21], v[38:39], v[52:53] op_sel:[0,1,0] op_sel_hi:[1,0,0]
	v_sub_f32_e32 v24, v46, v48
	v_sub_f32_e32 v18, v14, v40
	v_mov_b32_e32 v20, v22
	v_mov_b32_e32 v21, v36
	v_mov_b32_e32 v22, v32
	v_mov_b32_e32 v23, v34

.LBB0_985:
	v_or_b32_e32 v14, 16, v6
	v_lshlrev_b32_e32 v7, 5, v14
	v_and_or_b32 v7, v7, s65, v30
	v_lshlrev_b32_e32 v194, 3, v7
	v_pk_mul_f32 v[24:25], v[176:177], s[28:29] op_sel_hi:[1,0]
	v_pk_mul_f32 v[18:19], v[174:175], s[28:29] op_sel_hi:[1,0]
	v_pk_mul_f32 v[22:23], v[172:173], s[28:29] op_sel_hi:[1,0]
	v_pk_mul_f32 v[20:21], v[170:171], s[28:29] op_sel_hi:[1,0]
	s_and_b64 vcc, exec, s[4:5]
	v_lshl_add_u64 v[16:17], s[18:19], 0, v[194:195]
	s_cbranch_vccnz .LBB0_987
	global_load_dwordx4 v[32:35], v[16:17], off
	global_load_dwordx4 v[36:39], v[16:17], off offset:16
	s_waitcnt vmcnt(1)
	v_mov_b32_e32 v224, v32
	v_mov_b32_e32 v225, v33
	v_mov_b32_e32 v226, v34
	v_mov_b32_e32 v227, v35
	v_pk_mul_f32 v[40:41], v[18:19], v[32:33] op_sel:[1,1] op_sel_hi:[1,0]
	v_mul_f32_e32 v42, v25, v35
	v_mul_f32_e32 v44, v25, v34
	s_waitcnt vmcnt(0)
	v_mov_b32_e32 v228, v36
	v_mov_b32_e32 v229, v37
	v_mov_b32_e32 v230, v38
	v_mov_b32_e32 v231, v39
	v_pk_mul_f32 v[48:49], v[20:21], v[36:37] op_sel:[1,1] op_sel_hi:[1,0]
	v_mul_f32_e32 v50, v23, v39
	v_mul_f32_e32 v52, v23, v38
	v_pk_mul_f32 v[12:13], v[18:19], v[32:33]
	v_pk_mul_f32 v[46:47], v[20:21], v[36:37]
	v_pk_fma_f32 v[18:19], v[18:19], v[32:33], v[40:41] op_sel_hi:[0,1,1]
	v_pk_fma_f32 v[32:33], v[24:25], v[34:35], v[42:43] op_sel_hi:[1,1,0] neg_lo:[0,0,1] neg_hi:[0,0,1]
	v_pk_fma_f32 v[34:35], v[24:25], v[34:35], v[44:45] op_sel:[0,1,0] op_sel_hi:[1,0,0]
	v_pk_fma_f32 v[20:21], v[20:21], v[36:37], v[48:49] op_sel_hi:[0,1,1]
	v_pk_fma_f32 v[24:25], v[22:23], v[38:39], v[50:51] op_sel_hi:[1,1,0] neg_lo:[0,0,1] neg_hi:[0,0,1]
	v_pk_fma_f32 v[36:37], v[22:23], v[38:39], v[52:53] op_sel:[0,1,0] op_sel_hi:[1,0,0]
	v_sub_f32_e32 v20, v46, v48
	v_sub_f32_e32 v18, v12, v40
	v_mov_b32_e32 v22, v24
	v_mov_b32_e32 v23, v36
	v_mov_b32_e32 v24, v32
	v_mov_b32_e32 v25, v34

.LBB0_991:
	v_pk_mul_f32 v[22:23], v[168:169], s[28:29] op_sel_hi:[1,0]
	v_pk_mul_f32 v[18:19], v[166:167], s[28:29] op_sel_hi:[1,0]
	v_pk_mul_f32 v[20:21], v[164:165], s[28:29] op_sel_hi:[1,0]
	s_and_b64 vcc, exec, s[4:5]
	v_pk_mul_f32 v[24:25], v[162:163], s[28:29] op_sel_hi:[1,0]
	s_cbranch_vccnz .LBB0_1055
	v_mov_b32_e32 v32, v224
	v_mov_b32_e32 v33, v225
	v_mov_b32_e32 v34, v226
	v_mov_b32_e32 v35, v227
	v_mov_b32_e32 v36, v228
	v_mov_b32_e32 v37, v229
	v_mov_b32_e32 v38, v230
	v_mov_b32_e32 v39, v231
	v_pk_mul_f32 v[40:41], v[18:19], v[32:33] op_sel:[1,1] op_sel_hi:[1,0]
	v_mul_f32_e32 v42, v23, v35
	v_mul_f32_e32 v44, v23, v34
	v_pk_mul_f32 v[48:49], v[24:25], v[36:37] op_sel:[1,1] op_sel_hi:[1,0]
	v_mul_f32_e32 v50, v21, v39
	v_mul_f32_e32 v52, v21, v38
	v_pk_mul_f32 v[16:17], v[18:19], v[32:33]
	v_pk_mul_f32 v[46:47], v[24:25], v[36:37]
	v_pk_fma_f32 v[18:19], v[18:19], v[32:33], v[40:41] op_sel_hi:[0,1,1]
	v_pk_fma_f32 v[32:33], v[22:23], v[34:35], v[42:43] op_sel_hi:[1,1,0] neg_lo:[0,0,1] neg_hi:[0,0,1]
	v_pk_fma_f32 v[34:35], v[22:23], v[34:35], v[44:45] op_sel:[0,1,0] op_sel_hi:[1,0,0]
	v_pk_fma_f32 v[24:25], v[24:25], v[36:37], v[48:49] op_sel_hi:[0,1,1]
	v_pk_fma_f32 v[22:23], v[20:21], v[38:39], v[50:51] op_sel_hi:[1,1,0] neg_lo:[0,0,1] neg_hi:[0,0,1]
	v_pk_fma_f32 v[36:37], v[20:21], v[38:39], v[52:53] op_sel:[0,1,0] op_sel_hi:[1,0,0]
	v_sub_f32_e32 v24, v46, v48
	v_sub_f32_e32 v18, v16, v40
	v_mov_b32_e32 v20, v22
	v_mov_b32_e32 v21, v36
	v_mov_b32_e32 v22, v32
	v_mov_b32_e32 v23, v34
	s_and_b64 vcc, exec, s[6:7]
	s_mov_b64 s[42:43], -1
	s_cbranch_vccz .LBB0_1056

.LBB0_995:
	v_or_b32_e32 v14, 32, v6
	v_lshlrev_b32_e32 v7, 5, v14
	v_and_or_b32 v7, v7, s66, v30
	v_lshlrev_b32_e32 v194, 3, v7
	v_pk_mul_f32 v[24:25], v[160:161], s[28:29] op_sel_hi:[1,0]
	v_pk_mul_f32 v[18:19], v[158:159], s[28:29] op_sel_hi:[1,0]
	v_pk_mul_f32 v[22:23], v[156:157], s[28:29] op_sel_hi:[1,0]
	v_pk_mul_f32 v[20:21], v[154:155], s[28:29] op_sel_hi:[1,0]
	s_and_b64 vcc, exec, s[4:5]
	v_lshl_add_u64 v[16:17], s[18:19], 0, v[194:195]
	s_cbranch_vccnz .LBB0_997
	global_load_dwordx4 v[32:35], v[16:17], off
	global_load_dwordx4 v[36:39], v[16:17], off offset:16
	s_waitcnt vmcnt(1)
	v_mov_b32_e32 v224, v32
	v_mov_b32_e32 v225, v33
	v_mov_b32_e32 v226, v34
	v_mov_b32_e32 v227, v35
	v_pk_mul_f32 v[40:41], v[18:19], v[32:33] op_sel:[1,1] op_sel_hi:[1,0]
	v_mul_f32_e32 v42, v25, v35
	v_mul_f32_e32 v44, v25, v34
	s_waitcnt vmcnt(0)
	v_mov_b32_e32 v228, v36
	v_mov_b32_e32 v229, v37
	v_mov_b32_e32 v230, v38
	v_mov_b32_e32 v231, v39
	v_pk_mul_f32 v[48:49], v[20:21], v[36:37] op_sel:[1,1] op_sel_hi:[1,0]
	v_mul_f32_e32 v50, v23, v39
	v_mul_f32_e32 v52, v23, v38
	v_pk_mul_f32 v[12:13], v[18:19], v[32:33]
	v_pk_mul_f32 v[46:47], v[20:21], v[36:37]
	v_pk_fma_f32 v[18:19], v[18:19], v[32:33], v[40:41] op_sel_hi:[0,1,1]
	v_pk_fma_f32 v[32:33], v[24:25], v[34:35], v[42:43] op_sel_hi:[1,1,0] neg_lo:[0,0,1] neg_hi:[0,0,1]
	v_pk_fma_f32 v[34:35], v[24:25], v[34:35], v[44:45] op_sel:[0,1,0] op_sel_hi:[1,0,0]
	v_pk_fma_f32 v[20:21], v[20:21], v[36:37], v[48:49] op_sel_hi:[0,1,1]
	v_pk_fma_f32 v[24:25], v[22:23], v[38:39], v[50:51] op_sel_hi:[1,1,0] neg_lo:[0,0,1] neg_hi:[0,0,1]
	v_pk_fma_f32 v[36:37], v[22:23], v[38:39], v[52:53] op_sel:[0,1,0] op_sel_hi:[1,0,0]
	v_sub_f32_e32 v20, v46, v48
	v_sub_f32_e32 v18, v12, v40
	v_mov_b32_e32 v22, v24
	v_mov_b32_e32 v23, v36
	v_mov_b32_e32 v24, v32
	v_mov_b32_e32 v25, v34

.LBB0_1001:
	v_pk_mul_f32 v[22:23], v[152:153], s[28:29] op_sel_hi:[1,0]
	v_pk_mul_f32 v[18:19], v[150:151], s[28:29] op_sel_hi:[1,0]
	v_pk_mul_f32 v[20:21], v[148:149], s[28:29] op_sel_hi:[1,0]
	s_and_b64 vcc, exec, s[4:5]
	v_pk_mul_f32 v[24:25], v[146:147], s[28:29] op_sel_hi:[1,0]
	s_cbranch_vccnz .LBB0_1057
	v_mov_b32_e32 v32, v224
	v_mov_b32_e32 v33, v225
	v_mov_b32_e32 v34, v226
	v_mov_b32_e32 v35, v227
	v_mov_b32_e32 v36, v228
	v_mov_b32_e32 v37, v229
	v_mov_b32_e32 v38, v230
	v_mov_b32_e32 v39, v231
	v_pk_mul_f32 v[40:41], v[18:19], v[32:33] op_sel:[1,1] op_sel_hi:[1,0]
	v_mul_f32_e32 v42, v23, v35
	v_mul_f32_e32 v44, v23, v34
	v_pk_mul_f32 v[48:49], v[24:25], v[36:37] op_sel:[1,1] op_sel_hi:[1,0]
	v_mul_f32_e32 v50, v21, v39
	v_mul_f32_e32 v52, v21, v38
	v_pk_mul_f32 v[16:17], v[18:19], v[32:33]
	v_pk_mul_f32 v[46:47], v[24:25], v[36:37]
	v_pk_fma_f32 v[18:19], v[18:19], v[32:33], v[40:41] op_sel_hi:[0,1,1]
	v_pk_fma_f32 v[32:33], v[22:23], v[34:35], v[42:43] op_sel_hi:[1,1,0] neg_lo:[0,0,1] neg_hi:[0,0,1]
	v_pk_fma_f32 v[34:35], v[22:23], v[34:35], v[44:45] op_sel:[0,1,0] op_sel_hi:[1,0,0]
	v_pk_fma_f32 v[24:25], v[24:25], v[36:37], v[48:49] op_sel_hi:[0,1,1]
	v_pk_fma_f32 v[22:23], v[20:21], v[38:39], v[50:51] op_sel_hi:[1,1,0] neg_lo:[0,0,1] neg_hi:[0,0,1]
	v_pk_fma_f32 v[36:37], v[20:21], v[38:39], v[52:53] op_sel:[0,1,0] op_sel_hi:[1,0,0]
	v_sub_f32_e32 v24, v46, v48
	v_sub_f32_e32 v18, v16, v40
	v_mov_b32_e32 v20, v22
	v_mov_b32_e32 v21, v36
	v_mov_b32_e32 v22, v32
	v_mov_b32_e32 v23, v34
	s_and_b64 vcc, exec, s[6:7]
	s_mov_b64 s[42:43], -1
	s_cbranch_vccz .LBB0_1058

.LBB0_1005:
	v_or_b32_e32 v14, 48, v6
	v_lshlrev_b32_e32 v7, 5, v14
	v_and_or_b32 v7, v7, s67, v30
	v_lshlrev_b32_e32 v194, 3, v7
	v_pk_mul_f32 v[24:25], v[144:145], s[28:29] op_sel_hi:[1,0]
	v_pk_mul_f32 v[18:19], v[142:143], s[28:29] op_sel_hi:[1,0]
	v_pk_mul_f32 v[22:23], v[140:141], s[28:29] op_sel_hi:[1,0]
	v_pk_mul_f32 v[20:21], v[138:139], s[28:29] op_sel_hi:[1,0]
	s_and_b64 vcc, exec, s[4:5]
	v_lshl_add_u64 v[16:17], s[18:19], 0, v[194:195]
	s_cbranch_vccnz .LBB0_1007
	global_load_dwordx4 v[32:35], v[16:17], off
	global_load_dwordx4 v[36:39], v[16:17], off offset:16
	s_waitcnt vmcnt(1)
	v_mov_b32_e32 v224, v32
	v_mov_b32_e32 v225, v33
	v_mov_b32_e32 v226, v34
	v_mov_b32_e32 v227, v35
	v_pk_mul_f32 v[40:41], v[18:19], v[32:33] op_sel:[1,1] op_sel_hi:[1,0]
	v_mul_f32_e32 v42, v25, v35
	v_mul_f32_e32 v44, v25, v34
	s_waitcnt vmcnt(0)
	v_mov_b32_e32 v228, v36
	v_mov_b32_e32 v229, v37
	v_mov_b32_e32 v230, v38
	v_mov_b32_e32 v231, v39
	v_pk_mul_f32 v[48:49], v[20:21], v[36:37] op_sel:[1,1] op_sel_hi:[1,0]
	v_mul_f32_e32 v50, v23, v39
	v_mul_f32_e32 v52, v23, v38
	v_pk_mul_f32 v[12:13], v[18:19], v[32:33]
	v_pk_mul_f32 v[46:47], v[20:21], v[36:37]
	v_pk_fma_f32 v[18:19], v[18:19], v[32:33], v[40:41] op_sel_hi:[0,1,1]
	v_pk_fma_f32 v[32:33], v[24:25], v[34:35], v[42:43] op_sel_hi:[1,1,0] neg_lo:[0,0,1] neg_hi:[0,0,1]
	v_pk_fma_f32 v[34:35], v[24:25], v[34:35], v[44:45] op_sel:[0,1,0] op_sel_hi:[1,0,0]
	v_pk_fma_f32 v[20:21], v[20:21], v[36:37], v[48:49] op_sel_hi:[0,1,1]
	v_pk_fma_f32 v[24:25], v[22:23], v[38:39], v[50:51] op_sel_hi:[1,1,0] neg_lo:[0,0,1] neg_hi:[0,0,1]
	v_pk_fma_f32 v[36:37], v[22:23], v[38:39], v[52:53] op_sel:[0,1,0] op_sel_hi:[1,0,0]
	v_sub_f32_e32 v20, v46, v48
	v_sub_f32_e32 v18, v12, v40
	v_mov_b32_e32 v22, v24
	v_mov_b32_e32 v23, v36
	v_mov_b32_e32 v24, v32
	v_mov_b32_e32 v25, v34

.LBB0_1011:
	v_pk_mul_f32 v[22:23], v[136:137], s[28:29] op_sel_hi:[1,0]
	v_pk_mul_f32 v[18:19], v[134:135], s[28:29] op_sel_hi:[1,0]
	v_pk_mul_f32 v[20:21], v[132:133], s[28:29] op_sel_hi:[1,0]
	s_and_b64 vcc, exec, s[4:5]
	v_pk_mul_f32 v[24:25], v[130:131], s[28:29] op_sel_hi:[1,0]
	s_cbranch_vccnz .LBB0_1059
	v_mov_b32_e32 v32, v224
	v_mov_b32_e32 v33, v225
	v_mov_b32_e32 v34, v226
	v_mov_b32_e32 v35, v227
	v_mov_b32_e32 v36, v228
	v_mov_b32_e32 v37, v229
	v_mov_b32_e32 v38, v230
	v_mov_b32_e32 v39, v231
	v_pk_mul_f32 v[40:41], v[18:19], v[32:33] op_sel:[1,1] op_sel_hi:[1,0]
	v_mul_f32_e32 v42, v23, v35
	v_mul_f32_e32 v44, v23, v34
	v_pk_mul_f32 v[48:49], v[24:25], v[36:37] op_sel:[1,1] op_sel_hi:[1,0]
	v_mul_f32_e32 v50, v21, v39
	v_mul_f32_e32 v52, v21, v38
	v_pk_mul_f32 v[16:17], v[18:19], v[32:33]
	v_pk_mul_f32 v[46:47], v[24:25], v[36:37]
	v_pk_fma_f32 v[18:19], v[18:19], v[32:33], v[40:41] op_sel_hi:[0,1,1]
	v_pk_fma_f32 v[32:33], v[22:23], v[34:35], v[42:43] op_sel_hi:[1,1,0] neg_lo:[0,0,1] neg_hi:[0,0,1]
	v_pk_fma_f32 v[34:35], v[22:23], v[34:35], v[44:45] op_sel:[0,1,0] op_sel_hi:[1,0,0]
	v_pk_fma_f32 v[24:25], v[24:25], v[36:37], v[48:49] op_sel_hi:[0,1,1]
	v_pk_fma_f32 v[22:23], v[20:21], v[38:39], v[50:51] op_sel_hi:[1,1,0] neg_lo:[0,0,1] neg_hi:[0,0,1]
	v_pk_fma_f32 v[36:37], v[20:21], v[38:39], v[52:53] op_sel:[0,1,0] op_sel_hi:[1,0,0]
	v_sub_f32_e32 v24, v46, v48
	v_sub_f32_e32 v18, v16, v40
	v_mov_b32_e32 v20, v22
	v_mov_b32_e32 v21, v36
	v_mov_b32_e32 v22, v32
	v_mov_b32_e32 v23, v34
	s_and_b64 vcc, exec, s[6:7]
	s_mov_b64 s[42:43], -1
	s_cbranch_vccz .LBB0_1060

.LBB0_1015:
	v_add_u32_e32 v14, 0x80, v6
	v_lshlrev_b32_e32 v7, 5, v14
	v_and_or_b32 v7, v7, s64, v30
	v_lshlrev_b32_e32 v194, 3, v7
	v_pk_mul_f32 v[24:25], v[128:129], s[28:29] op_sel_hi:[1,0]
	v_pk_mul_f32 v[18:19], v[126:127], s[28:29] op_sel_hi:[1,0]
	v_pk_mul_f32 v[22:23], v[124:125], s[28:29] op_sel_hi:[1,0]
	v_pk_mul_f32 v[20:21], v[122:123], s[28:29] op_sel_hi:[1,0]
	s_and_b64 vcc, exec, s[4:5]
	v_lshl_add_u64 v[16:17], s[18:19], 0, v[194:195]
	s_cbranch_vccnz .LBB0_1017
	global_load_dwordx4 v[32:35], v[16:17], off
	global_load_dwordx4 v[36:39], v[16:17], off offset:16
	s_waitcnt vmcnt(1)
	v_mov_b32_e32 v224, v32
	v_mov_b32_e32 v225, v33
	v_mov_b32_e32 v226, v34
	v_mov_b32_e32 v227, v35
	v_pk_mul_f32 v[40:41], v[18:19], v[32:33] op_sel:[1,1] op_sel_hi:[1,0]
	v_mul_f32_e32 v42, v25, v35
	v_mul_f32_e32 v44, v25, v34
	s_waitcnt vmcnt(0)
	v_mov_b32_e32 v228, v36
	v_mov_b32_e32 v229, v37
	v_mov_b32_e32 v230, v38
	v_mov_b32_e32 v231, v39
	v_pk_mul_f32 v[48:49], v[20:21], v[36:37] op_sel:[1,1] op_sel_hi:[1,0]
	v_mul_f32_e32 v50, v23, v39
	v_mul_f32_e32 v52, v23, v38
	v_pk_mul_f32 v[12:13], v[18:19], v[32:33]
	v_pk_mul_f32 v[46:47], v[20:21], v[36:37]
	v_pk_fma_f32 v[18:19], v[18:19], v[32:33], v[40:41] op_sel_hi:[0,1,1]
	v_pk_fma_f32 v[32:33], v[24:25], v[34:35], v[42:43] op_sel_hi:[1,1,0] neg_lo:[0,0,1] neg_hi:[0,0,1]
	v_pk_fma_f32 v[34:35], v[24:25], v[34:35], v[44:45] op_sel:[0,1,0] op_sel_hi:[1,0,0]
	v_pk_fma_f32 v[20:21], v[20:21], v[36:37], v[48:49] op_sel_hi:[0,1,1]
	v_pk_fma_f32 v[24:25], v[22:23], v[38:39], v[50:51] op_sel_hi:[1,1,0] neg_lo:[0,0,1] neg_hi:[0,0,1]
	v_pk_fma_f32 v[36:37], v[22:23], v[38:39], v[52:53] op_sel:[0,1,0] op_sel_hi:[1,0,0]
	v_sub_f32_e32 v20, v46, v48
	v_sub_f32_e32 v18, v12, v40
	v_mov_b32_e32 v22, v24
	v_mov_b32_e32 v23, v36
	v_mov_b32_e32 v24, v32
	v_mov_b32_e32 v25, v34

.LBB0_1021:
	v_pk_mul_f32 v[22:23], v[120:121], s[28:29] op_sel_hi:[1,0]
	v_pk_mul_f32 v[18:19], v[118:119], s[28:29] op_sel_hi:[1,0]
	v_pk_mul_f32 v[20:21], v[116:117], s[28:29] op_sel_hi:[1,0]
	s_and_b64 vcc, exec, s[4:5]
	v_pk_mul_f32 v[24:25], v[114:115], s[28:29] op_sel_hi:[1,0]
	s_cbranch_vccnz .LBB0_1061
	v_mov_b32_e32 v32, v224
	v_mov_b32_e32 v33, v225
	v_mov_b32_e32 v34, v226
	v_mov_b32_e32 v35, v227
	v_mov_b32_e32 v36, v228
	v_mov_b32_e32 v37, v229
	v_mov_b32_e32 v38, v230
	v_mov_b32_e32 v39, v231
	v_pk_mul_f32 v[40:41], v[18:19], v[32:33] op_sel:[1,1] op_sel_hi:[1,0]
	v_mul_f32_e32 v42, v23, v35
	v_mul_f32_e32 v44, v23, v34
	v_pk_mul_f32 v[48:49], v[24:25], v[36:37] op_sel:[1,1] op_sel_hi:[1,0]
	v_mul_f32_e32 v50, v21, v39
	v_mul_f32_e32 v52, v21, v38
	v_pk_mul_f32 v[16:17], v[18:19], v[32:33]
	v_pk_mul_f32 v[46:47], v[24:25], v[36:37]
	v_pk_fma_f32 v[18:19], v[18:19], v[32:33], v[40:41] op_sel_hi:[0,1,1]
	v_pk_fma_f32 v[32:33], v[22:23], v[34:35], v[42:43] op_sel_hi:[1,1,0] neg_lo:[0,0,1] neg_hi:[0,0,1]
	v_pk_fma_f32 v[34:35], v[22:23], v[34:35], v[44:45] op_sel:[0,1,0] op_sel_hi:[1,0,0]
	v_pk_fma_f32 v[24:25], v[24:25], v[36:37], v[48:49] op_sel_hi:[0,1,1]
	v_pk_fma_f32 v[22:23], v[20:21], v[38:39], v[50:51] op_sel_hi:[1,1,0] neg_lo:[0,0,1] neg_hi:[0,0,1]
	v_pk_fma_f32 v[36:37], v[20:21], v[38:39], v[52:53] op_sel:[0,1,0] op_sel_hi:[1,0,0]
	v_sub_f32_e32 v24, v46, v48
	v_sub_f32_e32 v18, v16, v40
	v_mov_b32_e32 v20, v22
	v_mov_b32_e32 v21, v36
	v_mov_b32_e32 v22, v32
	v_mov_b32_e32 v23, v34
	s_and_b64 vcc, exec, s[6:7]
	s_mov_b64 s[42:43], -1
	s_cbranch_vccz .LBB0_1062

.LBB0_1025:
	v_add_u32_e32 v14, 0x90, v6
	v_lshlrev_b32_e32 v7, 5, v14
	v_and_or_b32 v7, v7, s65, v30
	v_lshlrev_b32_e32 v194, 3, v7
	v_pk_mul_f32 v[24:25], v[112:113], s[28:29] op_sel_hi:[1,0]
	v_pk_mul_f32 v[18:19], v[110:111], s[28:29] op_sel_hi:[1,0]
	v_pk_mul_f32 v[22:23], v[108:109], s[28:29] op_sel_hi:[1,0]
	v_pk_mul_f32 v[20:21], v[106:107], s[28:29] op_sel_hi:[1,0]
	s_and_b64 vcc, exec, s[4:5]
	v_lshl_add_u64 v[16:17], s[18:19], 0, v[194:195]
	s_cbranch_vccnz .LBB0_1027
	global_load_dwordx4 v[32:35], v[16:17], off
	global_load_dwordx4 v[36:39], v[16:17], off offset:16
	s_waitcnt vmcnt(1)
	v_mov_b32_e32 v224, v32
	v_mov_b32_e32 v225, v33
	v_mov_b32_e32 v226, v34
	v_mov_b32_e32 v227, v35
	v_pk_mul_f32 v[40:41], v[18:19], v[32:33] op_sel:[1,1] op_sel_hi:[1,0]
	v_mul_f32_e32 v42, v25, v35
	v_mul_f32_e32 v44, v25, v34
	s_waitcnt vmcnt(0)
	v_mov_b32_e32 v228, v36
	v_mov_b32_e32 v229, v37
	v_mov_b32_e32 v230, v38
	v_mov_b32_e32 v231, v39
	v_pk_mul_f32 v[48:49], v[20:21], v[36:37] op_sel:[1,1] op_sel_hi:[1,0]
	v_mul_f32_e32 v50, v23, v39
	v_mul_f32_e32 v52, v23, v38
	v_pk_mul_f32 v[12:13], v[18:19], v[32:33]
	v_pk_mul_f32 v[46:47], v[20:21], v[36:37]
	v_pk_fma_f32 v[18:19], v[18:19], v[32:33], v[40:41] op_sel_hi:[0,1,1]
	v_pk_fma_f32 v[32:33], v[24:25], v[34:35], v[42:43] op_sel_hi:[1,1,0] neg_lo:[0,0,1] neg_hi:[0,0,1]
	v_pk_fma_f32 v[34:35], v[24:25], v[34:35], v[44:45] op_sel:[0,1,0] op_sel_hi:[1,0,0]
	v_pk_fma_f32 v[20:21], v[20:21], v[36:37], v[48:49] op_sel_hi:[0,1,1]
	v_pk_fma_f32 v[24:25], v[22:23], v[38:39], v[50:51] op_sel_hi:[1,1,0] neg_lo:[0,0,1] neg_hi:[0,0,1]
	v_pk_fma_f32 v[36:37], v[22:23], v[38:39], v[52:53] op_sel:[0,1,0] op_sel_hi:[1,0,0]
	v_sub_f32_e32 v20, v46, v48
	v_sub_f32_e32 v18, v12, v40
	v_mov_b32_e32 v22, v24
	v_mov_b32_e32 v23, v36
	v_mov_b32_e32 v24, v32
	v_mov_b32_e32 v25, v34

.LBB0_1031:
	v_pk_mul_f32 v[22:23], v[104:105], s[28:29] op_sel_hi:[1,0]
	v_pk_mul_f32 v[18:19], v[102:103], s[28:29] op_sel_hi:[1,0]
	v_pk_mul_f32 v[20:21], v[100:101], s[28:29] op_sel_hi:[1,0]
	s_and_b64 vcc, exec, s[4:5]
	v_pk_mul_f32 v[24:25], v[98:99], s[28:29] op_sel_hi:[1,0]
	s_cbranch_vccnz .LBB0_1063
	v_mov_b32_e32 v32, v224
	v_mov_b32_e32 v33, v225
	v_mov_b32_e32 v34, v226
	v_mov_b32_e32 v35, v227
	v_mov_b32_e32 v36, v228
	v_mov_b32_e32 v37, v229
	v_mov_b32_e32 v38, v230
	v_mov_b32_e32 v39, v231
	v_pk_mul_f32 v[40:41], v[18:19], v[32:33] op_sel:[1,1] op_sel_hi:[1,0]
	v_mul_f32_e32 v42, v23, v35
	v_mul_f32_e32 v44, v23, v34
	v_pk_mul_f32 v[48:49], v[24:25], v[36:37] op_sel:[1,1] op_sel_hi:[1,0]
	v_mul_f32_e32 v50, v21, v39
	v_mul_f32_e32 v52, v21, v38
	v_pk_mul_f32 v[16:17], v[18:19], v[32:33]
	v_pk_mul_f32 v[46:47], v[24:25], v[36:37]
	v_pk_fma_f32 v[18:19], v[18:19], v[32:33], v[40:41] op_sel_hi:[0,1,1]
	v_pk_fma_f32 v[32:33], v[22:23], v[34:35], v[42:43] op_sel_hi:[1,1,0] neg_lo:[0,0,1] neg_hi:[0,0,1]
	v_pk_fma_f32 v[34:35], v[22:23], v[34:35], v[44:45] op_sel:[0,1,0] op_sel_hi:[1,0,0]
	v_pk_fma_f32 v[24:25], v[24:25], v[36:37], v[48:49] op_sel_hi:[0,1,1]
	v_pk_fma_f32 v[22:23], v[20:21], v[38:39], v[50:51] op_sel_hi:[1,1,0] neg_lo:[0,0,1] neg_hi:[0,0,1]
	v_pk_fma_f32 v[36:37], v[20:21], v[38:39], v[52:53] op_sel:[0,1,0] op_sel_hi:[1,0,0]
	v_sub_f32_e32 v24, v46, v48
	v_sub_f32_e32 v18, v16, v40
	v_mov_b32_e32 v20, v22
	v_mov_b32_e32 v21, v36
	v_mov_b32_e32 v22, v32
	v_mov_b32_e32 v23, v34
	s_and_b64 vcc, exec, s[6:7]
	s_mov_b64 s[42:43], -1
	s_cbranch_vccz .LBB0_1064

.LBB0_1035:
	v_add_u32_e32 v14, 0xa0, v6
	v_lshlrev_b32_e32 v7, 5, v14
	v_and_or_b32 v7, v7, s66, v30
	v_lshlrev_b32_e32 v194, 3, v7
	v_pk_mul_f32 v[24:25], v[96:97], s[28:29] op_sel_hi:[1,0]
	v_pk_mul_f32 v[18:19], v[94:95], s[28:29] op_sel_hi:[1,0]
	v_pk_mul_f32 v[22:23], v[92:93], s[28:29] op_sel_hi:[1,0]
	v_pk_mul_f32 v[20:21], v[90:91], s[28:29] op_sel_hi:[1,0]
	s_and_b64 vcc, exec, s[4:5]
	v_lshl_add_u64 v[16:17], s[18:19], 0, v[194:195]
	s_cbranch_vccnz .LBB0_1037
	global_load_dwordx4 v[32:35], v[16:17], off
	global_load_dwordx4 v[36:39], v[16:17], off offset:16
	s_waitcnt vmcnt(1)
	v_mov_b32_e32 v224, v32
	v_mov_b32_e32 v225, v33
	v_mov_b32_e32 v226, v34
	v_mov_b32_e32 v227, v35
	v_pk_mul_f32 v[40:41], v[18:19], v[32:33] op_sel:[1,1] op_sel_hi:[1,0]
	v_mul_f32_e32 v42, v25, v35
	v_mul_f32_e32 v44, v25, v34
	s_waitcnt vmcnt(0)
	v_mov_b32_e32 v228, v36
	v_mov_b32_e32 v229, v37
	v_mov_b32_e32 v230, v38
	v_mov_b32_e32 v231, v39
	v_pk_mul_f32 v[48:49], v[20:21], v[36:37] op_sel:[1,1] op_sel_hi:[1,0]
	v_mul_f32_e32 v50, v23, v39
	v_mul_f32_e32 v52, v23, v38
	v_pk_mul_f32 v[12:13], v[18:19], v[32:33]
	v_pk_mul_f32 v[46:47], v[20:21], v[36:37]
	v_pk_fma_f32 v[18:19], v[18:19], v[32:33], v[40:41] op_sel_hi:[0,1,1]
	v_pk_fma_f32 v[32:33], v[24:25], v[34:35], v[42:43] op_sel_hi:[1,1,0] neg_lo:[0,0,1] neg_hi:[0,0,1]
	v_pk_fma_f32 v[34:35], v[24:25], v[34:35], v[44:45] op_sel:[0,1,0] op_sel_hi:[1,0,0]
	v_pk_fma_f32 v[20:21], v[20:21], v[36:37], v[48:49] op_sel_hi:[0,1,1]
	v_pk_fma_f32 v[24:25], v[22:23], v[38:39], v[50:51] op_sel_hi:[1,1,0] neg_lo:[0,0,1] neg_hi:[0,0,1]
	v_pk_fma_f32 v[36:37], v[22:23], v[38:39], v[52:53] op_sel:[0,1,0] op_sel_hi:[1,0,0]
	v_sub_f32_e32 v20, v46, v48
	v_sub_f32_e32 v18, v12, v40
	v_mov_b32_e32 v22, v24
	v_mov_b32_e32 v23, v36
	v_mov_b32_e32 v24, v32
	v_mov_b32_e32 v25, v34

.LBB0_1041:
	v_pk_mul_f32 v[22:23], v[88:89], s[28:29] op_sel_hi:[1,0]
	v_pk_mul_f32 v[18:19], v[86:87], s[28:29] op_sel_hi:[1,0]
	v_pk_mul_f32 v[20:21], v[84:85], s[28:29] op_sel_hi:[1,0]
	s_and_b64 vcc, exec, s[4:5]
	v_pk_mul_f32 v[24:25], v[82:83], s[28:29] op_sel_hi:[1,0]
	s_cbranch_vccnz .LBB0_1065
	v_mov_b32_e32 v32, v224
	v_mov_b32_e32 v33, v225
	v_mov_b32_e32 v34, v226
	v_mov_b32_e32 v35, v227
	v_mov_b32_e32 v36, v228
	v_mov_b32_e32 v37, v229
	v_mov_b32_e32 v38, v230
	v_mov_b32_e32 v39, v231
	v_pk_mul_f32 v[40:41], v[18:19], v[32:33] op_sel:[1,1] op_sel_hi:[1,0]
	v_mul_f32_e32 v42, v23, v35
	v_mul_f32_e32 v44, v23, v34
	v_pk_mul_f32 v[48:49], v[24:25], v[36:37] op_sel:[1,1] op_sel_hi:[1,0]
	v_mul_f32_e32 v50, v21, v39
	v_mul_f32_e32 v52, v21, v38
	v_pk_mul_f32 v[16:17], v[18:19], v[32:33]
	v_pk_mul_f32 v[46:47], v[24:25], v[36:37]
	v_pk_fma_f32 v[18:19], v[18:19], v[32:33], v[40:41] op_sel_hi:[0,1,1]
	v_pk_fma_f32 v[32:33], v[22:23], v[34:35], v[42:43] op_sel_hi:[1,1,0] neg_lo:[0,0,1] neg_hi:[0,0,1]
	v_pk_fma_f32 v[34:35], v[22:23], v[34:35], v[44:45] op_sel:[0,1,0] op_sel_hi:[1,0,0]
	v_pk_fma_f32 v[24:25], v[24:25], v[36:37], v[48:49] op_sel_hi:[0,1,1]
	v_pk_fma_f32 v[22:23], v[20:21], v[38:39], v[50:51] op_sel_hi:[1,1,0] neg_lo:[0,0,1] neg_hi:[0,0,1]
	v_pk_fma_f32 v[36:37], v[20:21], v[38:39], v[52:53] op_sel:[0,1,0] op_sel_hi:[1,0,0]
	v_sub_f32_e32 v24, v46, v48
	v_sub_f32_e32 v18, v16, v40
	v_mov_b32_e32 v20, v22
	v_mov_b32_e32 v21, v36
	v_mov_b32_e32 v22, v32
	v_mov_b32_e32 v23, v34
	s_and_b64 vcc, exec, s[6:7]
	s_mov_b64 s[42:43], -1
	s_cbranch_vccz .LBB0_1066

.LBB0_1045:
	v_add_u32_e32 v18, 0xb0, v6
	v_lshlrev_b32_e32 v6, 5, v18
	v_and_or_b32 v6, v6, s67, v30
	v_lshlrev_b32_e32 v194, 3, v6
	v_pk_mul_f32 v[22:23], v[80:81], s[28:29] op_sel_hi:[1,0]
	v_pk_mul_f32 v[14:15], v[78:79], s[28:29] op_sel_hi:[1,0]
	v_pk_mul_f32 v[20:21], v[76:77], s[28:29] op_sel_hi:[1,0]
	v_pk_mul_f32 v[16:17], v[74:75], s[28:29] op_sel_hi:[1,0]
	s_and_b64 vcc, exec, s[4:5]
	v_lshl_add_u64 v[12:13], s[18:19], 0, v[194:195]
	s_cbranch_vccnz .LBB0_1047
	global_load_dwordx4 v[30:33], v[12:13], off
	global_load_dwordx4 v[34:37], v[12:13], off offset:16
	s_waitcnt vmcnt(1)
	v_mov_b32_e32 v224, v30
	v_mov_b32_e32 v225, v31
	v_mov_b32_e32 v226, v32
	v_mov_b32_e32 v227, v33
	v_pk_mul_f32 v[24:25], v[14:15], v[30:31] op_sel:[1,1] op_sel_hi:[1,0]
	v_mul_f32_e32 v38, v23, v33
	v_mul_f32_e32 v40, v23, v32
	s_waitcnt vmcnt(0)
	v_mov_b32_e32 v228, v34
	v_mov_b32_e32 v229, v35
	v_mov_b32_e32 v230, v36
	v_mov_b32_e32 v231, v37
	v_pk_mul_f32 v[44:45], v[16:17], v[34:35] op_sel:[1,1] op_sel_hi:[1,0]
	v_mul_f32_e32 v46, v21, v37
	v_mul_f32_e32 v48, v21, v36
	v_pk_mul_f32 v[6:7], v[14:15], v[30:31]
	v_pk_mul_f32 v[42:43], v[16:17], v[34:35]
	v_pk_fma_f32 v[14:15], v[14:15], v[30:31], v[24:25] op_sel_hi:[0,1,1]
	v_pk_fma_f32 v[30:31], v[22:23], v[32:33], v[38:39] op_sel_hi:[1,1,0] neg_lo:[0,0,1] neg_hi:[0,0,1]
	v_pk_fma_f32 v[32:33], v[22:23], v[32:33], v[40:41] op_sel:[0,1,0] op_sel_hi:[1,0,0]
	v_pk_fma_f32 v[16:17], v[16:17], v[34:35], v[44:45] op_sel_hi:[0,1,1]
	v_pk_fma_f32 v[22:23], v[20:21], v[36:37], v[46:47] op_sel_hi:[1,1,0] neg_lo:[0,0,1] neg_hi:[0,0,1]
	v_pk_fma_f32 v[34:35], v[20:21], v[36:37], v[48:49] op_sel:[0,1,0] op_sel_hi:[1,0,0]
	v_sub_f32_e32 v16, v42, v44
	v_sub_f32_e32 v14, v6, v24
	v_mov_b32_e32 v20, v22
	v_mov_b32_e32 v21, v34
	v_mov_b32_e32 v22, v30
	v_mov_b32_e32 v23, v32

.LBB0_1051:
	v_pk_mul_f32 v[16:17], v[72:73], s[28:29] op_sel_hi:[1,0]
	v_pk_mul_f32 v[10:11], v[70:71], s[28:29] op_sel_hi:[1,0]
	v_pk_mul_f32 v[14:15], v[68:69], s[28:29] op_sel_hi:[1,0]
	s_and_b64 vcc, exec, s[4:5]
	v_pk_mul_f32 v[18:19], v[66:67], s[28:29] op_sel_hi:[1,0]
	s_cbranch_vccnz .LBB0_1067
	v_mov_b32_e32 v20, v224
	v_mov_b32_e32 v21, v225
	v_mov_b32_e32 v22, v226
	v_mov_b32_e32 v23, v227
	v_mov_b32_e32 v30, v228
	v_mov_b32_e32 v31, v229
	v_mov_b32_e32 v32, v230
	v_mov_b32_e32 v33, v231
	v_pk_mul_f32 v[24:25], v[10:11], v[20:21] op_sel:[1,1] op_sel_hi:[1,0]
	v_mul_f32_e32 v34, v17, v23
	v_mul_f32_e32 v36, v17, v22
	v_pk_mul_f32 v[40:41], v[18:19], v[30:31] op_sel:[1,1] op_sel_hi:[1,0]
	v_mul_f32_e32 v42, v15, v33
	v_mul_f32_e32 v44, v15, v32
	v_pk_mul_f32 v[12:13], v[10:11], v[20:21]
	v_pk_mul_f32 v[38:39], v[18:19], v[30:31]
	v_pk_fma_f32 v[10:11], v[10:11], v[20:21], v[24:25] op_sel_hi:[0,1,1]
	v_pk_fma_f32 v[20:21], v[16:17], v[22:23], v[34:35] op_sel_hi:[1,1,0] neg_lo:[0,0,1] neg_hi:[0,0,1]
	v_pk_fma_f32 v[22:23], v[16:17], v[22:23], v[36:37] op_sel:[0,1,0] op_sel_hi:[1,0,0]
	v_pk_fma_f32 v[18:19], v[18:19], v[30:31], v[40:41] op_sel_hi:[0,1,1]
	v_pk_fma_f32 v[16:17], v[14:15], v[32:33], v[42:43] op_sel_hi:[1,1,0] neg_lo:[0,0,1] neg_hi:[0,0,1]
	v_pk_fma_f32 v[30:31], v[14:15], v[32:33], v[44:45] op_sel:[0,1,0] op_sel_hi:[1,0,0]
	v_sub_f32_e32 v18, v38, v40
	v_sub_f32_e32 v10, v12, v24
	v_mov_b32_e32 v14, v16
	v_mov_b32_e32 v15, v30
	v_mov_b32_e32 v16, v20
	v_mov_b32_e32 v17, v22
	s_and_b64 vcc, exec, s[6:7]
	s_mov_b64 s[4:5], -1
	s_cbranch_vccz .LBB0_1068
